# P3 K-loop LDS-DMA pieces to scalar-base form as well (all four GEMM K-loops now address every piece as scalar base + 32-bit lane offset)
# baseline (speedup 1.0000x reference)
.Lp3_first:
	ds_read_b128 v[184:187], v174
	ds_read_b128 v[188:191], v175
	ds_read_b128 v[192:195], v174 offset:2048
	ds_read_b128 v[196:199], v175 offset:2048
	ds_read_b128 v[200:203], v174 offset:16384
	ds_read_b128 v[204:207], v175 offset:16384
	ds_read_b128 v[208:211], v174 offset:18432
	ds_read_b128 v[212:215], v175 offset:18432
	s_add_u32 s78, s16, s28
	s_addc_u32 s79, s17, s29
	s_add_i32 m0, s39, 0x8000
	ds_read_b128 v[216:219], v177
	ds_read_b128 v[220:223], v177 offset:2048
	ds_read_b128 v[224:227], v178
	ds_read_b128 v[228:231], v178 offset:2048
	ds_read_b128 v[232:235], v177 offset:4096
	ds_read_b128 v[236:239], v177 offset:6144
	ds_read_b128 v[240:243], v178 offset:4096
	ds_read_b128 v[244:247], v178 offset:6144
	global_load_lds_dwordx4 v150, s[78:79]
	s_add_i32 m0, s39, 0xa000
	s_nop 0
	global_load_lds_dwordx4 v130, s[78:79]
	s_add_i32 m0, s39, 0xc000
	s_nop 0
	global_load_lds_dwordx4 v132, s[78:79]
	s_add_i32 m0, s39, 0xe000
	s_nop 0
	global_load_lds_dwordx4 v134, s[78:79]
	s_waitcnt vmcnt(8)
	s_waitcnt lgkmcnt(0)
	s_barrier
	s_setprio 1
	s_waitcnt lgkmcnt(0)
	v_mfma_f32_16x16x32_bf16 v[126:129], v[184:187], v[216:219], 0
	s_add_u32 s34, s2, s28
	s_addc_u32 s35, s3, s29
	s_add_u32 s77, s34, 0x63000100
	s_addc_u32 s78, s35, 0
	v_mfma_f32_16x16x32_bf16 v[122:125], v[192:195], v[216:219], 0
	s_and_b64 s[34:35], s[30:31], exec
	s_cselect_b32 s35, s7, s78
	s_cselect_b32 s34, s6, s77
	s_add_u32 s77, s25, s28
	v_mfma_f32_16x16x32_bf16 v[118:121], v[184:187], v[220:223], 0
	s_addc_u32 s78, s75, s29
	s_and_b64 s[30:31], s[30:31], exec
	s_cselect_b32 s31, s27, s78
	s_cselect_b32 s30, s26, s77
	v_mfma_f32_16x16x32_bf16 v[114:117], v[192:195], v[220:223], 0
	v_mfma_f32_16x16x32_bf16 v[110:113], v[184:187], v[232:235], 0
	v_mfma_f32_16x16x32_bf16 v[102:105], v[192:195], v[232:235], 0
	v_mfma_f32_16x16x32_bf16 v[94:97], v[184:187], v[236:239], 0
	v_mfma_f32_16x16x32_bf16 v[86:89], v[192:195], v[236:239], 0
	v_mfma_f32_16x16x32_bf16 v[126:129], v[188:191], v[224:227], v[126:129]
	v_mfma_f32_16x16x32_bf16 v[122:125], v[196:199], v[224:227], v[122:125]
	v_mfma_f32_16x16x32_bf16 v[118:121], v[188:191], v[228:231], v[118:121]
	v_mfma_f32_16x16x32_bf16 v[114:117], v[196:199], v[228:231], v[114:117]
	v_mfma_f32_16x16x32_bf16 v[110:113], v[188:191], v[240:243], v[110:113]
	v_mfma_f32_16x16x32_bf16 v[102:105], v[196:199], v[240:243], v[102:105]
	v_mfma_f32_16x16x32_bf16 v[94:97], v[188:191], v[244:247], v[94:97]
	v_mfma_f32_16x16x32_bf16 v[86:89], v[196:199], v[244:247], v[86:89]
	s_setprio 0
	s_setprio 1
	v_mfma_f32_16x16x32_bf16 v[106:109], v[200:203], v[216:219], 0
	v_mfma_f32_16x16x32_bf16 v[98:101], v[208:211], v[216:219], 0
	v_mfma_f32_16x16x32_bf16 v[90:93], v[200:203], v[220:223], 0
	v_mfma_f32_16x16x32_bf16 v[82:85], v[208:211], v[220:223], 0
	v_mfma_f32_16x16x32_bf16 v[78:81], v[200:203], v[232:235], 0
	v_mfma_f32_16x16x32_bf16 v[74:77], v[208:211], v[232:235], 0
	v_mfma_f32_16x16x32_bf16 v[70:73], v[200:203], v[236:239], 0
	v_mfma_f32_16x16x32_bf16 v[66:69], v[208:211], v[236:239], 0
	v_mfma_f32_16x16x32_bf16 v[106:109], v[204:207], v[224:227], v[106:109]
	v_mfma_f32_16x16x32_bf16 v[98:101], v[212:215], v[224:227], v[98:101]
	v_mfma_f32_16x16x32_bf16 v[90:93], v[204:207], v[228:231], v[90:93]
	v_mfma_f32_16x16x32_bf16 v[82:85], v[212:215], v[228:231], v[82:85]
	v_mfma_f32_16x16x32_bf16 v[78:81], v[204:207], v[240:243], v[78:81]
	v_mfma_f32_16x16x32_bf16 v[74:77], v[212:215], v[240:243], v[74:77]
	v_mfma_f32_16x16x32_bf16 v[70:73], v[204:207], v[244:247], v[70:73]
	v_mfma_f32_16x16x32_bf16 v[66:69], v[212:215], v[244:247], v[66:69]
	s_setprio 0
	s_barrier
	s_add_i32 s77, s45, s33
	s_mov_b32 m0, s77
	ds_read_b128 v[216:219], v177 offset:16384
	ds_read_b128 v[220:223], v177 offset:18432
	ds_read_b128 v[224:227], v178 offset:16384
	ds_read_b128 v[228:231], v178 offset:18432
	ds_read_b128 v[232:235], v177 offset:20480
	ds_read_b128 v[236:239], v177 offset:22528
	ds_read_b128 v[240:243], v178 offset:20480
	ds_read_b128 v[244:247], v178 offset:22528
	global_load_lds_dwordx4 v146, s[30:31]
	s_add_i32 m0, s77, 0x2000
	s_add_u32 s78, s30, 0x80000
	s_addc_u32 s79, s31, 0
	s_add_i32 s77, s47, s33
	global_load_lds_dwordx4 v148, s[30:31]
	s_mov_b32 m0, s77
	s_nop 0
	global_load_lds_dwordx4 v146, s[78:79]
	s_add_i32 m0, s77, 0x2000
	s_nop 0
	global_load_lds_dwordx4 v148, s[78:79]
	s_waitcnt vmcnt(6)
	s_waitcnt lgkmcnt(0)
	s_barrier
	s_setprio 1
	s_waitcnt lgkmcnt(0)
	v_mfma_f32_16x16x32_bf16 v[62:65], v[184:187], v[216:219], 0
	v_mfma_f32_16x16x32_bf16 v[58:61], v[192:195], v[216:219], 0
	v_mfma_f32_16x16x32_bf16 v[50:53], v[184:187], v[220:223], 0
	v_mfma_f32_16x16x32_bf16 v[42:45], v[192:195], v[220:223], 0
	v_mfma_f32_16x16x32_bf16 v[34:37], v[184:187], v[232:235], 0
	v_mfma_f32_16x16x32_bf16 v[26:29], v[192:195], v[232:235], 0
	v_mfma_f32_16x16x32_bf16 v[18:21], v[184:187], v[236:239], 0
	v_mfma_f32_16x16x32_bf16 v[10:13], v[192:195], v[236:239], 0
	v_mfma_f32_16x16x32_bf16 v[62:65], v[188:191], v[224:227], v[62:65]
	v_mfma_f32_16x16x32_bf16 v[58:61], v[196:199], v[224:227], v[58:61]
	v_mfma_f32_16x16x32_bf16 v[50:53], v[188:191], v[228:231], v[50:53]
	v_mfma_f32_16x16x32_bf16 v[42:45], v[196:199], v[228:231], v[42:45]
	v_mfma_f32_16x16x32_bf16 v[34:37], v[188:191], v[240:243], v[34:37]
	v_mfma_f32_16x16x32_bf16 v[26:29], v[196:199], v[240:243], v[26:29]
	v_mfma_f32_16x16x32_bf16 v[18:21], v[188:191], v[244:247], v[18:21]
	v_mfma_f32_16x16x32_bf16 v[10:13], v[196:199], v[244:247], v[10:13]
	s_setprio 0
	s_setprio 1
	v_mfma_f32_16x16x32_bf16 v[54:57], v[200:203], v[216:219], 0
	v_mfma_f32_16x16x32_bf16 v[46:49], v[208:211], v[216:219], 0
	v_mfma_f32_16x16x32_bf16 v[38:41], v[200:203], v[220:223], 0
	v_mfma_f32_16x16x32_bf16 v[30:33], v[208:211], v[220:223], 0
	v_mfma_f32_16x16x32_bf16 v[22:25], v[200:203], v[232:235], 0
	v_mfma_f32_16x16x32_bf16 v[14:17], v[208:211], v[232:235], 0
	v_mfma_f32_16x16x32_bf16 v[6:9], v[200:203], v[236:239], 0
	v_mfma_f32_16x16x32_bf16 v[2:5], v[208:211], v[236:239], 0
	v_mfma_f32_16x16x32_bf16 v[54:57], v[204:207], v[224:227], v[54:57]
	v_mfma_f32_16x16x32_bf16 v[46:49], v[212:215], v[224:227], v[46:49]
	v_mfma_f32_16x16x32_bf16 v[38:41], v[204:207], v[228:231], v[38:41]
	v_mfma_f32_16x16x32_bf16 v[30:33], v[212:215], v[228:231], v[30:33]
	v_mfma_f32_16x16x32_bf16 v[22:25], v[204:207], v[240:243], v[22:25]
	v_mfma_f32_16x16x32_bf16 v[14:17], v[212:215], v[240:243], v[14:17]
	v_mfma_f32_16x16x32_bf16 v[6:9], v[204:207], v[244:247], v[6:9]
	v_mfma_f32_16x16x32_bf16 v[2:5], v[212:215], v[244:247], v[2:5]
	s_setprio 0
	s_barrier
	s_branch .Lp3_blk3

.LBB0_385:
	s_cmp_eq_u32 s28, 0
	s_cbranch_scc1 .Lp3_first
	ds_read_b128 v[184:187], v174
	ds_read_b128 v[188:191], v175
	ds_read_b128 v[192:195], v174 offset:2048
	ds_read_b128 v[196:199], v175 offset:2048
	ds_read_b128 v[200:203], v174 offset:16384
	ds_read_b128 v[204:207], v175 offset:16384
	ds_read_b128 v[208:211], v174 offset:18432
	ds_read_b128 v[212:215], v175 offset:18432
	s_add_u32 s78, s16, s28
	s_addc_u32 s79, s17, s29
	s_add_i32 m0, s39, 0x8000
	ds_read_b128 v[216:219], v177
	ds_read_b128 v[220:223], v177 offset:2048
	ds_read_b128 v[224:227], v178
	ds_read_b128 v[228:231], v178 offset:2048
	ds_read_b128 v[232:235], v177 offset:4096
	ds_read_b128 v[236:239], v177 offset:6144
	ds_read_b128 v[240:243], v178 offset:4096
	ds_read_b128 v[244:247], v178 offset:6144
	global_load_lds_dwordx4 v150, s[78:79]
	s_add_i32 m0, s39, 0xa000
	s_nop 0
	global_load_lds_dwordx4 v130, s[78:79]
	s_add_i32 m0, s39, 0xc000
	s_nop 0
	global_load_lds_dwordx4 v132, s[78:79]
	s_add_i32 m0, s39, 0xe000
	s_nop 0
	global_load_lds_dwordx4 v134, s[78:79]
	s_waitcnt vmcnt(8)
	s_waitcnt lgkmcnt(0)
	s_barrier
	s_setprio 1
	s_waitcnt lgkmcnt(0)
	v_mfma_f32_16x16x32_bf16 v[126:129], v[184:187], v[216:219], v[126:129]
	s_add_u32 s34, s2, s28
	s_addc_u32 s35, s3, s29
	s_add_u32 s77, s34, 0x63000100
	s_addc_u32 s78, s35, 0
	v_mfma_f32_16x16x32_bf16 v[122:125], v[192:195], v[216:219], v[122:125]
	s_and_b64 s[34:35], s[30:31], exec
	s_cselect_b32 s35, s7, s78
	s_cselect_b32 s34, s6, s77
	s_add_u32 s77, s25, s28
	v_mfma_f32_16x16x32_bf16 v[118:121], v[184:187], v[220:223], v[118:121]
	s_addc_u32 s78, s75, s29
	s_and_b64 s[30:31], s[30:31], exec
	s_cselect_b32 s31, s27, s78
	s_cselect_b32 s30, s26, s77
	v_mfma_f32_16x16x32_bf16 v[114:117], v[192:195], v[220:223], v[114:117]
	v_mfma_f32_16x16x32_bf16 v[110:113], v[184:187], v[232:235], v[110:113]
	v_mfma_f32_16x16x32_bf16 v[102:105], v[192:195], v[232:235], v[102:105]
	v_mfma_f32_16x16x32_bf16 v[94:97], v[184:187], v[236:239], v[94:97]
	v_mfma_f32_16x16x32_bf16 v[86:89], v[192:195], v[236:239], v[86:89]
	v_mfma_f32_16x16x32_bf16 v[126:129], v[188:191], v[224:227], v[126:129]
	v_mfma_f32_16x16x32_bf16 v[122:125], v[196:199], v[224:227], v[122:125]
	v_mfma_f32_16x16x32_bf16 v[118:121], v[188:191], v[228:231], v[118:121]
	v_mfma_f32_16x16x32_bf16 v[114:117], v[196:199], v[228:231], v[114:117]
	v_mfma_f32_16x16x32_bf16 v[110:113], v[188:191], v[240:243], v[110:113]
	v_mfma_f32_16x16x32_bf16 v[102:105], v[196:199], v[240:243], v[102:105]
	v_mfma_f32_16x16x32_bf16 v[94:97], v[188:191], v[244:247], v[94:97]
	v_mfma_f32_16x16x32_bf16 v[86:89], v[196:199], v[244:247], v[86:89]
	s_setprio 0
	s_setprio 1
	v_mfma_f32_16x16x32_bf16 v[106:109], v[200:203], v[216:219], v[106:109]
	v_mfma_f32_16x16x32_bf16 v[98:101], v[208:211], v[216:219], v[98:101]
	v_mfma_f32_16x16x32_bf16 v[90:93], v[200:203], v[220:223], v[90:93]
	v_mfma_f32_16x16x32_bf16 v[82:85], v[208:211], v[220:223], v[82:85]
	v_mfma_f32_16x16x32_bf16 v[78:81], v[200:203], v[232:235], v[78:81]
	v_mfma_f32_16x16x32_bf16 v[74:77], v[208:211], v[232:235], v[74:77]
	v_mfma_f32_16x16x32_bf16 v[70:73], v[200:203], v[236:239], v[70:73]
	v_mfma_f32_16x16x32_bf16 v[66:69], v[208:211], v[236:239], v[66:69]
	v_mfma_f32_16x16x32_bf16 v[106:109], v[204:207], v[224:227], v[106:109]
	v_mfma_f32_16x16x32_bf16 v[98:101], v[212:215], v[224:227], v[98:101]
	v_mfma_f32_16x16x32_bf16 v[90:93], v[204:207], v[228:231], v[90:93]
	v_mfma_f32_16x16x32_bf16 v[82:85], v[212:215], v[228:231], v[82:85]
	v_mfma_f32_16x16x32_bf16 v[78:81], v[204:207], v[240:243], v[78:81]
	v_mfma_f32_16x16x32_bf16 v[74:77], v[212:215], v[240:243], v[74:77]
	v_mfma_f32_16x16x32_bf16 v[70:73], v[204:207], v[244:247], v[70:73]
	v_mfma_f32_16x16x32_bf16 v[66:69], v[212:215], v[244:247], v[66:69]
	s_setprio 0
	s_barrier
	s_add_i32 s77, s45, s33
	s_mov_b32 m0, s77
	ds_read_b128 v[216:219], v177 offset:16384
	ds_read_b128 v[220:223], v177 offset:18432
	ds_read_b128 v[224:227], v178 offset:16384
	ds_read_b128 v[228:231], v178 offset:18432
	ds_read_b128 v[232:235], v177 offset:20480
	ds_read_b128 v[236:239], v177 offset:22528
	ds_read_b128 v[240:243], v178 offset:20480
	ds_read_b128 v[244:247], v178 offset:22528
	global_load_lds_dwordx4 v146, s[30:31]
	s_add_i32 m0, s77, 0x2000
	s_add_u32 s78, s30, 0x80000
	s_addc_u32 s79, s31, 0
	s_add_i32 s77, s47, s33
	global_load_lds_dwordx4 v148, s[30:31]
	s_mov_b32 m0, s77
	s_nop 0
	global_load_lds_dwordx4 v146, s[78:79]
	s_add_i32 m0, s77, 0x2000
	s_nop 0
	global_load_lds_dwordx4 v148, s[78:79]
	s_waitcnt vmcnt(6)
	s_waitcnt lgkmcnt(0)
	s_barrier
	s_setprio 1
	s_waitcnt lgkmcnt(0)
	v_mfma_f32_16x16x32_bf16 v[62:65], v[184:187], v[216:219], v[62:65]
	v_mfma_f32_16x16x32_bf16 v[58:61], v[192:195], v[216:219], v[58:61]
	v_mfma_f32_16x16x32_bf16 v[50:53], v[184:187], v[220:223], v[50:53]
	v_mfma_f32_16x16x32_bf16 v[42:45], v[192:195], v[220:223], v[42:45]
	v_mfma_f32_16x16x32_bf16 v[34:37], v[184:187], v[232:235], v[34:37]
	v_mfma_f32_16x16x32_bf16 v[26:29], v[192:195], v[232:235], v[26:29]
	v_mfma_f32_16x16x32_bf16 v[18:21], v[184:187], v[236:239], v[18:21]
	v_mfma_f32_16x16x32_bf16 v[10:13], v[192:195], v[236:239], v[10:13]
	v_mfma_f32_16x16x32_bf16 v[62:65], v[188:191], v[224:227], v[62:65]
	v_mfma_f32_16x16x32_bf16 v[58:61], v[196:199], v[224:227], v[58:61]
	v_mfma_f32_16x16x32_bf16 v[50:53], v[188:191], v[228:231], v[50:53]
	v_mfma_f32_16x16x32_bf16 v[42:45], v[196:199], v[228:231], v[42:45]
	v_mfma_f32_16x16x32_bf16 v[34:37], v[188:191], v[240:243], v[34:37]
	v_mfma_f32_16x16x32_bf16 v[26:29], v[196:199], v[240:243], v[26:29]
	v_mfma_f32_16x16x32_bf16 v[18:21], v[188:191], v[244:247], v[18:21]
	v_mfma_f32_16x16x32_bf16 v[10:13], v[196:199], v[244:247], v[10:13]
	s_setprio 0
	s_setprio 1
	v_mfma_f32_16x16x32_bf16 v[54:57], v[200:203], v[216:219], v[54:57]
	v_mfma_f32_16x16x32_bf16 v[46:49], v[208:211], v[216:219], v[46:49]
	v_mfma_f32_16x16x32_bf16 v[38:41], v[200:203], v[220:223], v[38:41]
	v_mfma_f32_16x16x32_bf16 v[30:33], v[208:211], v[220:223], v[30:33]
	v_mfma_f32_16x16x32_bf16 v[22:25], v[200:203], v[232:235], v[22:25]
	v_mfma_f32_16x16x32_bf16 v[14:17], v[208:211], v[232:235], v[14:17]
	v_mfma_f32_16x16x32_bf16 v[6:9], v[200:203], v[236:239], v[6:9]
	v_mfma_f32_16x16x32_bf16 v[2:5], v[208:211], v[236:239], v[2:5]
	v_mfma_f32_16x16x32_bf16 v[54:57], v[204:207], v[224:227], v[54:57]
	v_mfma_f32_16x16x32_bf16 v[46:49], v[212:215], v[224:227], v[46:49]
	v_mfma_f32_16x16x32_bf16 v[38:41], v[204:207], v[228:231], v[38:41]
	v_mfma_f32_16x16x32_bf16 v[30:33], v[212:215], v[228:231], v[30:33]
	v_mfma_f32_16x16x32_bf16 v[22:25], v[204:207], v[240:243], v[22:25]
	v_mfma_f32_16x16x32_bf16 v[14:17], v[212:215], v[240:243], v[14:17]
	v_mfma_f32_16x16x32_bf16 v[6:9], v[204:207], v[244:247], v[6:9]
	v_mfma_f32_16x16x32_bf16 v[2:5], v[212:215], v[244:247], v[2:5]
	s_setprio 0
	s_barrier
.Lp3_blk3:
	ds_read_b128 v[184:187], v174 offset:32768
	ds_read_b128 v[188:191], v175 offset:32768
	ds_read_b128 v[192:195], v174 offset:34816
	ds_read_b128 v[196:199], v175 offset:34816
	ds_read_b128 v[200:203], v174 offset:49152
	ds_read_b128 v[204:207], v175 offset:49152
	ds_read_b128 v[208:211], v174 offset:51200
	ds_read_b128 v[212:215], v175 offset:51200
	s_mov_b32 m0, s39
	ds_read_b128 v[216:219], v177 offset:32768
	ds_read_b128 v[220:223], v177 offset:34816
	ds_read_b128 v[224:227], v178 offset:32768
	ds_read_b128 v[228:231], v178 offset:34816
	ds_read_b128 v[232:235], v177 offset:36864
	ds_read_b128 v[236:239], v177 offset:38912
	ds_read_b128 v[240:243], v178 offset:36864
	ds_read_b128 v[244:247], v178 offset:38912
	global_load_lds_dwordx4 v166, s[34:35]
	s_mov_b32 m0, s40
	s_nop 0
	global_load_lds_dwordx4 v164, s[34:35]
	s_mov_b32 m0, s41
	s_nop 0
	global_load_lds_dwordx4 v162, s[34:35]
	s_mov_b32 m0, s42
	s_nop 0
	global_load_lds_dwordx4 v160, s[34:35]
	s_waitcnt vmcnt(8)
	s_waitcnt lgkmcnt(0)
	s_barrier
	s_setprio 1
	s_waitcnt lgkmcnt(0)
	v_mfma_f32_16x16x32_bf16 v[126:129], v[184:187], v[216:219], v[126:129]
	v_mfma_f32_16x16x32_bf16 v[122:125], v[192:195], v[216:219], v[122:125]
	v_mfma_f32_16x16x32_bf16 v[118:121], v[184:187], v[220:223], v[118:121]
	v_mfma_f32_16x16x32_bf16 v[114:117], v[192:195], v[220:223], v[114:117]
	v_mfma_f32_16x16x32_bf16 v[110:113], v[184:187], v[232:235], v[110:113]
	v_mfma_f32_16x16x32_bf16 v[102:105], v[192:195], v[232:235], v[102:105]
	v_mfma_f32_16x16x32_bf16 v[94:97], v[184:187], v[236:239], v[94:97]
	v_mfma_f32_16x16x32_bf16 v[86:89], v[192:195], v[236:239], v[86:89]
	v_mfma_f32_16x16x32_bf16 v[126:129], v[188:191], v[224:227], v[126:129]
	v_mfma_f32_16x16x32_bf16 v[122:125], v[196:199], v[224:227], v[122:125]
	v_mfma_f32_16x16x32_bf16 v[118:121], v[188:191], v[228:231], v[118:121]
	v_mfma_f32_16x16x32_bf16 v[114:117], v[196:199], v[228:231], v[114:117]
	v_mfma_f32_16x16x32_bf16 v[110:113], v[188:191], v[240:243], v[110:113]
	v_mfma_f32_16x16x32_bf16 v[102:105], v[196:199], v[240:243], v[102:105]
	v_mfma_f32_16x16x32_bf16 v[94:97], v[188:191], v[244:247], v[94:97]
	v_mfma_f32_16x16x32_bf16 v[86:89], v[196:199], v[244:247], v[86:89]
	s_setprio 0
	s_setprio 1
	v_mfma_f32_16x16x32_bf16 v[106:109], v[200:203], v[216:219], v[106:109]
	v_mfma_f32_16x16x32_bf16 v[98:101], v[208:211], v[216:219], v[98:101]
	v_mfma_f32_16x16x32_bf16 v[90:93], v[200:203], v[220:223], v[90:93]
	v_mfma_f32_16x16x32_bf16 v[82:85], v[208:211], v[220:223], v[82:85]
	v_mfma_f32_16x16x32_bf16 v[78:81], v[200:203], v[232:235], v[78:81]
	v_mfma_f32_16x16x32_bf16 v[74:77], v[208:211], v[232:235], v[74:77]
	v_mfma_f32_16x16x32_bf16 v[70:73], v[200:203], v[236:239], v[70:73]
	v_mfma_f32_16x16x32_bf16 v[66:69], v[208:211], v[236:239], v[66:69]
	v_mfma_f32_16x16x32_bf16 v[106:109], v[204:207], v[224:227], v[106:109]
	v_mfma_f32_16x16x32_bf16 v[98:101], v[212:215], v[224:227], v[98:101]
	v_mfma_f32_16x16x32_bf16 v[90:93], v[204:207], v[228:231], v[90:93]
	v_mfma_f32_16x16x32_bf16 v[82:85], v[212:215], v[228:231], v[82:85]
	v_mfma_f32_16x16x32_bf16 v[78:81], v[204:207], v[240:243], v[78:81]
	v_mfma_f32_16x16x32_bf16 v[74:77], v[212:215], v[240:243], v[74:77]
	v_mfma_f32_16x16x32_bf16 v[70:73], v[204:207], v[244:247], v[70:73]
	v_mfma_f32_16x16x32_bf16 v[66:69], v[212:215], v[244:247], v[66:69]
	s_setprio 0
	s_barrier
	s_add_i32 s34, s65, s33
	s_add_u32 s78, s30, s8
	s_addc_u32 s79, s31, s9
	s_mov_b32 m0, s34
	ds_read_b128 v[160:163], v177 offset:49152
	ds_read_b128 v[164:167], v177 offset:51200
	ds_read_b128 v[216:219], v178 offset:49152
	ds_read_b128 v[220:223], v178 offset:51200
	ds_read_b128 v[224:227], v177 offset:53248
	ds_read_b128 v[228:231], v177 offset:55296
	ds_read_b128 v[232:235], v178 offset:53248
	ds_read_b128 v[236:239], v178 offset:55296
	global_load_lds_dwordx4 v146, s[78:79]
	s_add_i32 m0, s34, 0x2000
	s_add_u32 s30, s30, 0x80080
	s_addc_u32 s31, s31, 0
	s_add_i32 s34, s67, s33
	global_load_lds_dwordx4 v148, s[78:79]
	s_mov_b32 m0, s34
	s_nop 0
	global_load_lds_dwordx4 v146, s[30:31]
	s_add_i32 m0, s34, 0x2000
	s_nop 0
	global_load_lds_dwordx4 v148, s[30:31]
	s_waitcnt vmcnt(6)
	s_waitcnt lgkmcnt(0)
	s_barrier
	s_setprio 1
	s_waitcnt lgkmcnt(0)
	v_mfma_f32_16x16x32_bf16 v[62:65], v[184:187], v[160:163], v[62:65]
	v_mfma_f32_16x16x32_bf16 v[58:61], v[192:195], v[160:163], v[58:61]
	v_mfma_f32_16x16x32_bf16 v[50:53], v[184:187], v[164:167], v[50:53]
	v_mfma_f32_16x16x32_bf16 v[42:45], v[192:195], v[164:167], v[42:45]
	v_mfma_f32_16x16x32_bf16 v[34:37], v[184:187], v[224:227], v[34:37]
	v_mfma_f32_16x16x32_bf16 v[26:29], v[192:195], v[224:227], v[26:29]
	v_mfma_f32_16x16x32_bf16 v[18:21], v[184:187], v[228:231], v[18:21]
	v_mfma_f32_16x16x32_bf16 v[10:13], v[192:195], v[228:231], v[10:13]
	v_mfma_f32_16x16x32_bf16 v[62:65], v[188:191], v[216:219], v[62:65]
	v_mfma_f32_16x16x32_bf16 v[58:61], v[196:199], v[216:219], v[58:61]
	v_mfma_f32_16x16x32_bf16 v[50:53], v[188:191], v[220:223], v[50:53]
	v_mfma_f32_16x16x32_bf16 v[42:45], v[196:199], v[220:223], v[42:45]
	v_mfma_f32_16x16x32_bf16 v[34:37], v[188:191], v[232:235], v[34:37]
	v_mfma_f32_16x16x32_bf16 v[26:29], v[196:199], v[232:235], v[26:29]
	v_mfma_f32_16x16x32_bf16 v[18:21], v[188:191], v[236:239], v[18:21]
	v_mfma_f32_16x16x32_bf16 v[10:13], v[196:199], v[236:239], v[10:13]
	s_setprio 0
	s_setprio 1
	v_mfma_f32_16x16x32_bf16 v[54:57], v[200:203], v[160:163], v[54:57]
	v_mfma_f32_16x16x32_bf16 v[46:49], v[208:211], v[160:163], v[46:49]
	v_mfma_f32_16x16x32_bf16 v[38:41], v[200:203], v[164:167], v[38:41]
	v_mfma_f32_16x16x32_bf16 v[30:33], v[208:211], v[164:167], v[30:33]
	v_mfma_f32_16x16x32_bf16 v[22:25], v[200:203], v[224:227], v[22:25]
	v_mfma_f32_16x16x32_bf16 v[14:17], v[208:211], v[224:227], v[14:17]
	v_mfma_f32_16x16x32_bf16 v[6:9], v[200:203], v[228:231], v[6:9]
	v_mfma_f32_16x16x32_bf16 v[2:5], v[208:211], v[228:231], v[2:5]
	v_mfma_f32_16x16x32_bf16 v[54:57], v[204:207], v[216:219], v[54:57]
	v_mfma_f32_16x16x32_bf16 v[46:49], v[212:215], v[216:219], v[46:49]
	v_mfma_f32_16x16x32_bf16 v[38:41], v[204:207], v[220:223], v[38:41]
	v_mfma_f32_16x16x32_bf16 v[30:33], v[212:215], v[220:223], v[30:33]
	v_mfma_f32_16x16x32_bf16 v[22:25], v[204:207], v[232:235], v[22:25]
	v_mfma_f32_16x16x32_bf16 v[14:17], v[212:215], v[232:235], v[14:17]
	v_mfma_f32_16x16x32_bf16 v[6:9], v[204:207], v[236:239], v[6:9]
	v_mfma_f32_16x16x32_bf16 v[2:5], v[212:215], v[236:239], v[2:5]
	s_setprio 0
	s_barrier
	s_add_i32 s76, s76, 2
	s_add_u32 s28, s28, 0x100
	s_addc_u32 s29, s29, 0
	s_cmp_gt_u32 s76, 29
	s_cbranch_scc1 .LBB0_389
